# v79 + M2/CB phases skip the redundant moe_prep scan (tables from M1 still in LDS)
# speedup vs baseline: 1.0069x; 1.0009x over previous
.LBB0_855:
	s_or_b64 exec, exec, s[0:1]
	s_waitcnt lgkmcnt(0)
	s_barrier
	s_getreg_b32 s0, hwreg(HW_REG_HW_ID, 0, 6)
	s_lshl_b32 s0, s0, 2
	s_add_i32 s0, s0, 0x27000
	v_mov_b32_e32 v0, s0
	ds_read_b32 v0, v0
	v_mov_b32_e32 v1, 0
	v_mov_b32_e32 v2, 0
	s_waitcnt lgkmcnt(0)
	v_readfirstlane_b32 s0, v0
	v_mbcnt_lo_u32_b32 v0, -1, v1
	v_mbcnt_hi_u32_b32 v0, -1, v0
	v_lshl_or_b32 v52, s0, 6, v0
	s_getreg_b32 s0, hwreg(HW_REG_HW_ID, 0, 6)
	s_lshl_b32 s0, s0, 2
	s_add_i32 s0, s0, 0x27000
	v_mov_b32_e32 v0, s0
	ds_read_b32 v0, v0
	v_mov_b32_e32 v1, 0
	s_waitcnt lgkmcnt(0)
	v_readfirstlane_b32 s0, v0
	v_mbcnt_lo_u32_b32 v0, -1, v2
	v_mbcnt_hi_u32_b32 v0, -1, v0
	v_lshl_or_b32 v0, s0, 6, v0
	s_movk_i32 s0, 0x100
	s_nop 0
	v_cmp_gt_i32_e32 vcc, s0, v0
	v_lshl_add_u32 v2, v0, 2, 0
	s_add_i32 s0, 0, 0x1f424
	v_mov_b32_e32 v0, s0
	s_waitcnt lgkmcnt(0)
	s_barrier
	ds_read_b32 v0, v0
	v_readlane_b32 s2, v253, 63
	v_readlane_b32 s3, v254, 0
	s_and_b64 vcc, exec, s[2:3]
	s_waitcnt lgkmcnt(0)
	v_readfirstlane_b32 s0, v0
	s_lshl_b32 s0, s0, 3
	s_cbranch_vccz .LBB0_896
	v_readlane_b32 s2, v253, 2
	s_mov_b32 s12, s72
	v_readlane_b32 s3, v253, 3
	s_mov_b32 s1, s2
	s_branch .LBB0_897

.LBB0_970:
	s_or_b64 exec, exec, s[0:1]
	s_waitcnt lgkmcnt(0)
	s_barrier
	s_getreg_b32 s0, hwreg(HW_REG_HW_ID, 0, 6)
	s_lshl_b32 s0, s0, 2
	s_add_i32 s0, s0, 0x27000
	v_mov_b32_e32 v0, s0
	ds_read_b32 v0, v0
	v_mov_b32_e32 v1, 0
	v_mov_b32_e32 v4, 0
	s_waitcnt lgkmcnt(0)
	v_readfirstlane_b32 s0, v0
	v_mbcnt_lo_u32_b32 v0, -1, v1
	v_mbcnt_hi_u32_b32 v0, -1, v0
	v_lshl_or_b32 v2, s0, 6, v0
	s_getreg_b32 s0, hwreg(HW_REG_HW_ID, 0, 6)
	s_lshl_b32 s0, s0, 2
	s_add_i32 s0, s0, 0x27000
	v_mov_b32_e32 v0, s0
	ds_read_b32 v0, v0
	v_mov_b32_e32 v1, 0
	s_waitcnt lgkmcnt(0)
	v_readfirstlane_b32 s0, v0
	v_mbcnt_lo_u32_b32 v0, -1, v1
	v_mbcnt_hi_u32_b32 v0, -1, v0
	v_lshl_or_b32 v3, s0, 6, v0
	s_getreg_b32 s0, hwreg(HW_REG_HW_ID, 0, 6)
	s_lshl_b32 s0, s0, 2
	s_add_i32 s0, s0, 0x27000
	v_mov_b32_e32 v0, s0
	ds_read_b32 v0, v0
	v_mov_b32_e32 v1, 0
	s_waitcnt lgkmcnt(0)
	v_readfirstlane_b32 s0, v0
	v_mbcnt_lo_u32_b32 v0, -1, v4
	v_mbcnt_hi_u32_b32 v0, -1, v0
	v_lshl_or_b32 v0, s0, 6, v0
	s_movk_i32 s0, 0x100
	s_nop 0
	v_cmp_gt_i32_e32 vcc, s0, v0
	v_lshl_add_u32 v4, v0, 2, 0
	v_ashrrev_i32_e32 v0, 6, v3
	v_readlane_b32 s0, v253, 30
	s_waitcnt lgkmcnt(0)
	s_barrier
	v_add_u32_e32 v80, s0, v0
	s_movk_i32 s0, 0x4000
	v_cmp_gt_i32_e32 vcc, s0, v80
	s_and_saveexec_b64 s[2:3], vcc
	s_cbranch_execz .LBB0_1014
	v_readlane_b32 s4, v253, 4
	v_and_b32_e32 v1, 63, v2
	v_readlane_b32 s5, v253, 5
	v_lshlrev_b32_e32 v2, 5, v1
	v_mov_b32_e32 v3, 0
	v_readlane_b32 s18, v253, 18
	v_readlane_b32 s19, v253, 19
	v_readlane_b32 s4, v254, 3
	v_lshl_add_u64 v[84:85], s[64:65], 0, v[2:3]
	v_lshl_add_u64 v[82:83], s[18:19], 0, v[2:3]
	v_lshlrev_b32_e32 v2, 4, v1
	v_readlane_b32 s5, v254, 4
	v_lshlrev_b32_e32 v0, 3, v0
	v_ashrrev_i32_e32 v81, 31, v80
	v_lshl_add_u64 v[86:87], s[4:5], 0, v[2:3]
	s_lshl_b32 s4, s72, 6
	v_cmp_gt_u32_e64 s[0:1], 8, v1
	v_add3_u32 v88, s4, v0, v1
	v_readlane_b32 s4, v253, 2
	v_lshlrev_b64 v[0:1], 11, v[80:81]
	v_readlane_b32 s9, v253, 9
	v_readlane_b32 s5, v253, 3
	v_or_b32_e32 v0, v0, v2
	v_readlane_b32 s6, v253, 6
	v_readlane_b32 s7, v253, 7
	v_readlane_b32 s8, v253, 8
	s_lshl_b32 s9, s4, 6
	v_lshl_add_u64 v[0:1], s[70:71], 0, v[0:1]
	s_mov_b64 s[4:5], 0xd60d500
	s_ashr_i32 s75, s74, 31
	v_lshl_add_u64 v[90:91], v[0:1], 0, s[4:5]
	s_lshl_b64 s[4:5], s[74:75], 11
	s_mov_b64 s[6:7], 0
	s_mov_b32 s8, 0x3fb504f3
	v_mov_b32_e32 v81, 0x3727c5ac
	v_readlane_b32 s10, v253, 10
	v_readlane_b32 s11, v253, 11
	v_readlane_b32 s12, v253, 12
	v_readlane_b32 s13, v253, 13
	v_readlane_b32 s14, v253, 14
	v_readlane_b32 s15, v253, 15
	v_readlane_b32 s16, v253, 16
	v_readlane_b32 s17, v253, 17
	global_load_dwordx4 v[200:203], v[82:83], off
	global_load_dwordx4 v[204:207], v[82:83], off offset:16
	global_load_dwordx4 v[208:211], v[84:85], off
	global_load_dwordx4 v[212:215], v[84:85], off offset:16
	global_load_dwordx4 v[216:219], v[82:83], off offset:2048
	global_load_dwordx4 v[220:223], v[82:83], off offset:2064
	global_load_dwordx4 v[224:227], v[84:85], off offset:2048
	global_load_dwordx4 v[228:231], v[84:85], off offset:2064
	s_waitcnt vmcnt(0)
	s_branch .LBB0_1012

.LBB0_2435:
	s_or_b64 exec, exec, s[0:1]
	s_waitcnt lgkmcnt(0)
	s_barrier
	s_getreg_b32 s0, hwreg(HW_REG_HW_ID, 0, 6)
	s_lshl_b32 s0, s0, 2
	s_add_i32 s0, s0, 0x27000
	v_mov_b32_e32 v0, s0
	ds_read_b32 v0, v0
	v_mov_b32_e32 v1, 0
	v_mov_b32_e32 v2, 0
	s_waitcnt lgkmcnt(0)
	v_readfirstlane_b32 s0, v0
	v_mbcnt_lo_u32_b32 v0, -1, v1
	v_mbcnt_hi_u32_b32 v0, -1, v0
	v_lshl_or_b32 v52, s0, 6, v0
	s_getreg_b32 s0, hwreg(HW_REG_HW_ID, 0, 6)
	s_lshl_b32 s0, s0, 2
	s_add_i32 s0, s0, 0x27000
	v_mov_b32_e32 v0, s0
	ds_read_b32 v0, v0
	v_mov_b32_e32 v1, 0
	s_waitcnt lgkmcnt(0)
	v_readfirstlane_b32 s0, v0
	v_mbcnt_lo_u32_b32 v0, -1, v2
	v_mbcnt_hi_u32_b32 v0, -1, v0
	v_lshl_or_b32 v0, s0, 6, v0
	s_movk_i32 s0, 0x100
	s_nop 0
	v_cmp_gt_i32_e32 vcc, s0, v0
	v_lshl_add_u32 v2, v0, 2, 0
	s_add_i32 s0, 0, 0x1f424
	v_mov_b32_e32 v0, s0
	s_waitcnt lgkmcnt(0)
	s_barrier
	ds_read_b32 v0, v0
	v_readlane_b32 s2, v253, 63
	v_readlane_b32 s3, v254, 0
	s_and_b64 vcc, exec, s[2:3]
	s_waitcnt lgkmcnt(0)
	v_readfirstlane_b32 s0, v0
	s_lshl_b32 s0, s0, 3
	s_cbranch_vccz .LBB0_2476
	v_readlane_b32 s2, v253, 2
	s_mov_b32 s12, s72
	v_readlane_b32 s3, v253, 3
	s_mov_b32 s1, s2
	s_cmp_ge_i32 s12, s0
	s_cbranch_scc0 .LBB0_2477
	s_branch .LBB0_2497

.LBB0_2549:
	s_or_b64 exec, exec, s[0:1]
	s_waitcnt lgkmcnt(0)
	s_barrier
	s_getreg_b32 s0, hwreg(HW_REG_HW_ID, 0, 6)
	s_lshl_b32 s0, s0, 2
	s_add_i32 s0, s0, 0x27000
	v_mov_b32_e32 v0, s0
	ds_read_b32 v0, v0
	v_mov_b32_e32 v1, 0
	v_mov_b32_e32 v4, 0
	s_waitcnt lgkmcnt(0)
	v_readfirstlane_b32 s0, v0
	v_mbcnt_lo_u32_b32 v0, -1, v1
	v_mbcnt_hi_u32_b32 v0, -1, v0
	v_lshl_or_b32 v2, s0, 6, v0
	s_getreg_b32 s0, hwreg(HW_REG_HW_ID, 0, 6)
	s_lshl_b32 s0, s0, 2
	s_add_i32 s0, s0, 0x27000
	v_mov_b32_e32 v0, s0
	ds_read_b32 v0, v0
	v_mov_b32_e32 v1, 0
	s_waitcnt lgkmcnt(0)
	v_readfirstlane_b32 s0, v0
	v_mbcnt_lo_u32_b32 v0, -1, v1
	v_mbcnt_hi_u32_b32 v0, -1, v0
	v_lshl_or_b32 v3, s0, 6, v0
	s_getreg_b32 s0, hwreg(HW_REG_HW_ID, 0, 6)
	s_lshl_b32 s0, s0, 2
	s_add_i32 s0, s0, 0x27000
	v_mov_b32_e32 v0, s0
	ds_read_b32 v0, v0
	v_mov_b32_e32 v1, 0
	s_waitcnt lgkmcnt(0)
	v_readfirstlane_b32 s0, v0
	v_mbcnt_lo_u32_b32 v0, -1, v4
	v_mbcnt_hi_u32_b32 v0, -1, v0
	v_lshl_or_b32 v0, s0, 6, v0
	s_movk_i32 s0, 0x100
	s_nop 0
	v_cmp_gt_i32_e32 vcc, s0, v0
	v_lshl_add_u32 v4, v0, 2, 0
	v_ashrrev_i32_e32 v0, 6, v3
	v_readlane_b32 s0, v253, 30
	s_waitcnt lgkmcnt(0)
	s_barrier
	v_add_u32_e32 v24, s0, v0
	s_movk_i32 s0, 0x4000
	v_cmp_gt_i32_e32 vcc, s0, v24
	s_and_saveexec_b64 s[0:1], vcc
	s_cbranch_execz .LBB0_2595
	v_readlane_b32 s0, v253, 4
	v_readlane_b32 s2, v253, 6
	v_readlane_b32 s14, v253, 18
	v_readlane_b32 s3, v253, 7
	v_readlane_b32 s15, v253, 19
	s_add_u32 s2, s14, 0x1000
	v_and_b32_e32 v1, 63, v2
	v_readlane_b32 s6, v253, 10
	s_addc_u32 s3, s15, 0
	v_lshlrev_b32_e32 v2, 5, v1
	v_mov_b32_e32 v3, 0
	v_readlane_b32 s7, v253, 11
	s_add_u32 s6, s64, 0x1000
	v_or_b32_e32 v4, 0x800, v2
	v_mov_b32_e32 v5, v3
	s_addc_u32 s7, s65, 0
	v_lshl_add_u64 v[26:27], s[2:3], 0, v[2:3]
	v_lshl_add_u64 v[30:31], s[2:3], 0, v[4:5]
	v_readlane_b32 s2, v254, 3
	v_readlane_b32 s12, v253, 16
	v_readlane_b32 s13, v253, 17
	s_cmp_lg_u64 s[66:67], 0
	v_lshl_add_u64 v[32:33], s[6:7], 0, v[4:5]
	v_lshlrev_b32_e32 v4, 4, v1
	v_readlane_b32 s3, v254, 4
	v_readlane_b32 s1, v253, 5
	s_cselect_b64 s[12:13], -1, 0
	v_lshl_add_u64 v[34:35], s[2:3], 0, v[4:5]
	s_lshl_b32 s2, s72, 6
	v_lshlrev_b32_e32 v0, 3, v0
	v_ashrrev_i32_e32 v25, 31, v24
	v_cmp_gt_u32_e64 s[0:1], 8, v1
	v_add3_u32 v36, s2, v0, v1
	v_readlane_b32 s2, v253, 2
	v_lshlrev_b64 v[0:1], 11, v[24:25]
	v_readlane_b32 s11, v253, 15
	v_readlane_b32 s3, v253, 3
	v_or_b32_e32 v0, v0, v4
	s_lshl_b32 s11, s2, 6
	v_lshl_add_u64 v[0:1], s[70:71], 0, v[0:1]
	s_mov_b64 s[2:3], 0xd60d900
	v_lshl_add_u64 v[38:39], v[0:1], 0, s[2:3]
	v_lshlrev_b64 v[0:1], 12, v[24:25]
	v_or_b32_e32 v0, v0, v2
	v_lshl_add_u64 v[0:1], s[66:67], 0, v[0:1]
	s_mov_b64 s[2:3], 0x800
	v_readlane_b32 s4, v253, 8
	v_readlane_b32 s5, v253, 9
	v_readlane_b32 s8, v253, 12
	v_readlane_b32 s9, v253, 13
	v_readlane_b32 s10, v253, 14
	s_ashr_i32 s75, s74, 31
	v_lshl_add_u64 v[40:41], v[0:1], 0, s[2:3]
	v_cndmask_b32_e64 v0, 0, 1, s[12:13]
	s_mov_b64 s[4:5], 0
	v_lshl_add_u64 v[28:29], s[6:7], 0, v[2:3]
	s_lshl_b64 s[6:7], s[74:75], 11
	s_lshl_b64 s[8:9], s[74:75], 12
	s_mov_b32 s10, 0x3fb504f3
	v_mov_b32_e32 v25, 0x3727c5ac
	s_mov_b32 s15, 0x800000
	s_movk_i32 s17, 0x3fff
	v_cmp_ne_u32_e64 s[2:3], 1, v0
	global_load_dwordx4 v[200:203], v[26:27], off
	global_load_dwordx4 v[204:207], v[28:29], off
	global_load_dwordx4 v[208:211], v[26:27], off offset:16
	global_load_dwordx4 v[212:215], v[28:29], off offset:16
	global_load_dwordx4 v[216:219], v[30:31], off
	global_load_dwordx4 v[220:223], v[32:33], off
	global_load_dwordx4 v[224:227], v[30:31], off offset:16
	global_load_dwordx4 v[228:231], v[32:33], off offset:16
	s_waitcnt vmcnt(0)
	s_branch .LBB0_2591
